# adds: P15 first K tile accumulates on srcC=0 (no zero-init movs)
# speedup vs baseline: 1.0292x; 1.0002x over previous
.LBB0_4277:
	ds_read_b128 v[10:13], v155
	ds_read_b128 v[170:173], v156
	ds_read_b128 v[6:9], v151
	ds_read_b128 v[178:181], v152
	ds_read_b128 v[174:177], v157
	ds_read_b128 v[182:185], v158
	ds_read_b128 v[186:189], v159
	ds_read_b128 v[190:193], v160
	s_ashr_i32 s31, s30, 31
	s_lshl_b64 s[36:37], s[30:31], 9
	s_add_u32 s36, s2, s36
	s_addc_u32 s37, s3, s37
	s_and_b64 s[38:39], s[4:5], exec
	s_cselect_b32 s49, s37, s43
	s_cselect_b32 s48, s36, s42
	s_ashr_i32 s35, s34, 31
	s_lshl_b64 s[38:39], s[34:35], 17
	s_add_u32 s38, s33, s38
	s_addc_u32 s39, s50, s39
	s_and_b64 s[46:47], s[4:5], exec
	s_cselect_b32 s47, s39, s45
	s_cselect_b32 s46, s38, s44
	s_add_u32 s70, s42, 0x10080
	s_addc_u32 s71, s43, 0
	s_add_i32 s35, s13, 0xc000
	v_lshl_add_u64 v[46:47], s[70:71], 0, v[134:135]
	s_mov_b32 m0, s35
	s_add_i32 s31, s13, 0xe000
	ds_read_b128 v[14:17], v167
	ds_read_b128 v[18:21], v167 offset:16
	ds_read_b128 v[22:25], v167 offset:2048
	ds_read_b128 v[26:29], v167 offset:2064
	ds_read_b128 v[30:33], v167 offset:4096
	ds_read_b128 v[34:37], v167 offset:4112
	ds_read_b128 v[38:41], v167 offset:6144
	ds_read_b128 v[42:45], v167 offset:6160
	global_load_lds_dwordx4 v[46:47], off
	v_lshl_add_u64 v[46:47], s[70:71], 0, v[140:141]
	s_mov_b32 m0, s31
	s_nop 0
	global_load_lds_dwordx4 v[46:47], off
	s_waitcnt vmcnt(8)
	s_waitcnt lgkmcnt(0)
	s_barrier
	s_setprio 1
	s_waitcnt lgkmcnt(0)
	v_mfma_f32_16x16x128_f8f6f4 v[130:133], v[6:13], v[14:21], 0
	v_mfma_f32_16x16x128_f8f6f4 v[122:125], v[170:177], v[14:21], 0
	v_mfma_f32_16x16x128_f8f6f4 v[114:117], v[6:13], v[22:29], 0
	v_mfma_f32_16x16x128_f8f6f4 v[106:109], v[170:177], v[22:29], 0
	v_mfma_f32_16x16x128_f8f6f4 v[98:101], v[6:13], v[30:37], 0
	v_mfma_f32_16x16x128_f8f6f4 v[90:93], v[170:177], v[30:37], 0
	v_mfma_f32_16x16x128_f8f6f4 v[74:77], v[6:13], v[38:45], 0
	v_mfma_f32_16x16x128_f8f6f4 v[58:61], v[170:177], v[38:45], 0
	s_setprio 0
	s_setprio 1
	v_mfma_f32_16x16x128_f8f6f4 v[126:129], v[178:185], v[14:21], 0
	v_mfma_f32_16x16x128_f8f6f4 v[118:121], v[186:193], v[14:21], 0
	v_mfma_f32_16x16x128_f8f6f4 v[110:113], v[178:185], v[22:29], 0
	v_mfma_f32_16x16x128_f8f6f4 v[102:105], v[186:193], v[22:29], 0
	v_mfma_f32_16x16x128_f8f6f4 v[94:97], v[178:185], v[30:37], 0
	v_mfma_f32_16x16x128_f8f6f4 v[86:89], v[186:193], v[30:37], 0
	v_mfma_f32_16x16x128_f8f6f4 v[62:65], v[178:185], v[38:45], 0
	v_mfma_f32_16x16x128_f8f6f4 v[54:57], v[186:193], v[38:45], 0
	s_setprio 0
	s_barrier
	v_lshl_add_u64 v[144:145], s[44:45], 0, v[136:137]
	s_mov_b32 m0, s51
	v_lshl_add_u64 v[14:15], v[144:145], 0, s[10:11]
	v_lshl_add_u64 v[146:147], s[44:45], 0, v[138:139]
	s_add_u32 s70, s44, 0x10100
	ds_read_b128 v[194:197], v167 offset:16384
	ds_read_b128 v[198:201], v167 offset:16400
	ds_read_b128 v[202:205], v167 offset:18432
	ds_read_b128 v[206:209], v167 offset:18448
	ds_read_b128 v[210:213], v167 offset:20480
	ds_read_b128 v[214:217], v167 offset:20496
	ds_read_b128 v[218:221], v167 offset:22528
	ds_read_b128 v[222:225], v167 offset:22544
	global_load_lds_dwordx4 v[14:15], off
	v_lshl_add_u64 v[14:15], v[146:147], 0, s[10:11]
	s_mov_b32 m0, s52
	s_addc_u32 s71, s45, 0
	global_load_lds_dwordx4 v[14:15], off
	v_lshl_add_u64 v[14:15], s[70:71], 0, v[136:137]
	s_mov_b32 m0, s53
	v_lshl_add_u64 v[148:149], s[42:43], 0, v[134:135]
	global_load_lds_dwordx4 v[14:15], off
	v_lshl_add_u64 v[14:15], s[70:71], 0, v[138:139]
	s_mov_b32 m0, s55
	v_lshl_add_u64 v[234:235], s[42:43], 0, v[140:141]
	global_load_lds_dwordx4 v[14:15], off
	v_lshl_add_u64 v[14:15], v[148:149], 0, s[10:11]
	s_mov_b32 m0, s13
	s_nop 0
	global_load_lds_dwordx4 v[14:15], off
	v_lshl_add_u64 v[14:15], v[234:235], 0, s[10:11]
	s_mov_b32 m0, s57
	s_nop 0
	global_load_lds_dwordx4 v[14:15], off
	s_waitcnt vmcnt(8)
	s_waitcnt lgkmcnt(0)
	s_barrier
	s_setprio 1
	s_waitcnt lgkmcnt(0)
	v_mfma_f32_16x16x128_f8f6f4 v[82:85], v[6:13], v[194:201], 0
	v_mfma_f32_16x16x128_f8f6f4 v[70:73], v[170:177], v[194:201], 0
	v_mfma_f32_16x16x128_f8f6f4 v[50:53], v[6:13], v[202:209], 0
	v_mfma_f32_16x16x128_f8f6f4 v[42:45], v[170:177], v[202:209], 0
	v_mfma_f32_16x16x128_f8f6f4 v[34:37], v[6:13], v[210:217], 0
	v_mfma_f32_16x16x128_f8f6f4 v[26:29], v[170:177], v[210:217], 0
	v_mfma_f32_16x16x128_f8f6f4 v[18:21], v[6:13], v[218:225], 0
	v_mfma_f32_16x16x128_f8f6f4 v[10:13], v[170:177], v[218:225], 0
	s_setprio 0
	s_setprio 1
	v_mfma_f32_16x16x128_f8f6f4 v[78:81], v[178:185], v[194:201], 0
	v_mfma_f32_16x16x128_f8f6f4 v[66:69], v[186:193], v[194:201], 0
	v_mfma_f32_16x16x128_f8f6f4 v[46:49], v[178:185], v[202:209], 0
	v_mfma_f32_16x16x128_f8f6f4 v[38:41], v[186:193], v[202:209], 0
	v_mfma_f32_16x16x128_f8f6f4 v[30:33], v[178:185], v[210:217], 0
	v_mfma_f32_16x16x128_f8f6f4 v[22:25], v[186:193], v[210:217], 0
	v_mfma_f32_16x16x128_f8f6f4 v[14:17], v[178:185], v[218:225], 0
	v_mfma_f32_16x16x128_f8f6f4 v[6:9], v[186:193], v[218:225], 0
	s_setprio 0
	s_barrier
	ds_read_b128 v[174:177], v161
	ds_read_b128 v[178:181], v162
	ds_read_b128 v[170:173], v153
	ds_read_b128 v[186:189], v154
	ds_read_b128 v[182:185], v163
	ds_read_b128 v[190:193], v164
	ds_read_b128 v[194:197], v165
	ds_read_b128 v[198:201], v166
	s_add_u32 s70, s42, 0x10100
	s_addc_u32 s71, s43, 0
	s_mov_b32 m0, s58
	v_lshl_add_u64 v[236:237], s[70:71], 0, v[134:135]
	ds_read_b128 v[202:205], v167 offset:32768
	ds_read_b128 v[206:209], v167 offset:32784
	ds_read_b128 v[210:213], v167 offset:34816
	ds_read_b128 v[214:217], v167 offset:34832
	ds_read_b128 v[218:221], v167 offset:36864
	ds_read_b128 v[222:225], v167 offset:36880
	ds_read_b128 v[226:229], v167 offset:38912
	ds_read_b128 v[230:233], v167 offset:38928
	global_load_lds_dwordx4 v[236:237], off
	v_lshl_add_u64 v[236:237], s[70:71], 0, v[140:141]
	s_mov_b32 m0, s59
	s_nop 0
	global_load_lds_dwordx4 v[236:237], off
	s_waitcnt vmcnt(8)
	s_waitcnt lgkmcnt(0)
	s_barrier
	s_setprio 1
	s_waitcnt lgkmcnt(0)
	v_mfma_f32_16x16x128_f8f6f4 v[130:133], v[170:177], v[202:209], v[130:133]
	v_mfma_f32_16x16x128_f8f6f4 v[122:125], v[178:185], v[202:209], v[122:125]
	v_mfma_f32_16x16x128_f8f6f4 v[114:117], v[170:177], v[210:217], v[114:117]
	v_mfma_f32_16x16x128_f8f6f4 v[106:109], v[178:185], v[210:217], v[106:109]
	v_mfma_f32_16x16x128_f8f6f4 v[98:101], v[170:177], v[218:225], v[98:101]
	v_mfma_f32_16x16x128_f8f6f4 v[90:93], v[178:185], v[218:225], v[90:93]
	v_mfma_f32_16x16x128_f8f6f4 v[74:77], v[170:177], v[226:233], v[74:77]
	v_mfma_f32_16x16x128_f8f6f4 v[58:61], v[178:185], v[226:233], v[58:61]
	s_setprio 0
	s_setprio 1
	v_mfma_f32_16x16x128_f8f6f4 v[126:129], v[186:193], v[202:209], v[126:129]
	v_mfma_f32_16x16x128_f8f6f4 v[118:121], v[194:201], v[202:209], v[118:121]
	v_mfma_f32_16x16x128_f8f6f4 v[110:113], v[186:193], v[210:217], v[110:113]
	v_mfma_f32_16x16x128_f8f6f4 v[102:105], v[194:201], v[210:217], v[102:105]
	v_mfma_f32_16x16x128_f8f6f4 v[94:97], v[186:193], v[218:225], v[94:97]
	v_mfma_f32_16x16x128_f8f6f4 v[86:89], v[194:201], v[218:225], v[86:89]
	v_mfma_f32_16x16x128_f8f6f4 v[62:65], v[186:193], v[226:233], v[62:65]
	v_mfma_f32_16x16x128_f8f6f4 v[54:57], v[194:201], v[226:233], v[54:57]
	s_setprio 0
	s_barrier
	s_mov_b32 m0, s61
	v_lshl_add_u64 v[144:145], v[144:145], 0, s[26:27]
	s_add_u32 s44, s44, 0x10180
	ds_read_b128 v[202:205], v167 offset:49152
	ds_read_b128 v[206:209], v167 offset:49168
	ds_read_b128 v[210:213], v167 offset:51200
	ds_read_b128 v[214:217], v167 offset:51216
	ds_read_b128 v[218:221], v167 offset:53248
	ds_read_b128 v[222:225], v167 offset:53264
	ds_read_b128 v[226:229], v167 offset:55296
	ds_read_b128 v[230:233], v167 offset:55312
	global_load_lds_dwordx4 v[144:145], off
	v_lshl_add_u64 v[144:145], v[146:147], 0, s[26:27]
	s_mov_b32 m0, s62
	s_addc_u32 s45, s45, 0
	global_load_lds_dwordx4 v[144:145], off
	v_lshl_add_u64 v[144:145], s[44:45], 0, v[136:137]
	s_mov_b32 m0, s65
	s_nop 0
	global_load_lds_dwordx4 v[144:145], off
	v_lshl_add_u64 v[144:145], s[44:45], 0, v[138:139]
	s_mov_b32 m0, s66
	s_nop 0
	global_load_lds_dwordx4 v[144:145], off
	v_lshl_add_u64 v[144:145], v[148:149], 0, s[26:27]
	s_mov_b32 m0, s63
	s_nop 0
	global_load_lds_dwordx4 v[144:145], off
	v_lshl_add_u64 v[144:145], v[234:235], 0, s[26:27]
	s_mov_b32 m0, s64
	s_nop 0
	global_load_lds_dwordx4 v[144:145], off
	s_waitcnt vmcnt(8)
	s_waitcnt lgkmcnt(0)
	s_barrier
	s_setprio 1
	s_waitcnt lgkmcnt(0)
	v_mfma_f32_16x16x128_f8f6f4 v[82:85], v[170:177], v[202:209], v[82:85]
	v_mfma_f32_16x16x128_f8f6f4 v[70:73], v[178:185], v[202:209], v[70:73]
	v_mfma_f32_16x16x128_f8f6f4 v[50:53], v[170:177], v[210:217], v[50:53]
	v_mfma_f32_16x16x128_f8f6f4 v[42:45], v[178:185], v[210:217], v[42:45]
	v_mfma_f32_16x16x128_f8f6f4 v[34:37], v[170:177], v[218:225], v[34:37]
	v_mfma_f32_16x16x128_f8f6f4 v[26:29], v[178:185], v[218:225], v[26:29]
	v_mfma_f32_16x16x128_f8f6f4 v[18:21], v[170:177], v[226:233], v[18:21]
	v_mfma_f32_16x16x128_f8f6f4 v[10:13], v[178:185], v[226:233], v[10:13]
	s_setprio 0
	s_setprio 1
	v_mfma_f32_16x16x128_f8f6f4 v[78:81], v[186:193], v[202:209], v[78:81]
	v_mfma_f32_16x16x128_f8f6f4 v[66:69], v[194:201], v[202:209], v[66:69]
	v_mfma_f32_16x16x128_f8f6f4 v[46:49], v[186:193], v[210:217], v[46:49]
	v_mfma_f32_16x16x128_f8f6f4 v[38:41], v[194:201], v[210:217], v[38:41]
	v_mfma_f32_16x16x128_f8f6f4 v[30:33], v[186:193], v[218:225], v[30:33]
	v_mfma_f32_16x16x128_f8f6f4 v[22:25], v[194:201], v[218:225], v[22:25]
	v_mfma_f32_16x16x128_f8f6f4 v[14:17], v[186:193], v[226:233], v[14:17]
	v_mfma_f32_16x16x128_f8f6f4 v[6:9], v[194:201], v[226:233], v[6:9]
	s_setprio 0
	s_barrier
	ds_read_b128 v[174:177], v155
	ds_read_b128 v[178:181], v156
	ds_read_b128 v[170:173], v151
	ds_read_b128 v[186:189], v152
	ds_read_b128 v[182:185], v157
	ds_read_b128 v[190:193], v158
	ds_read_b128 v[194:197], v159
	ds_read_b128 v[198:201], v160
	s_add_u32 s42, s42, 0x10180
	s_addc_u32 s43, s43, 0
	s_mov_b32 m0, s35
	v_lshl_add_u64 v[144:145], s[42:43], 0, v[134:135]
	ds_read_b128 v[202:205], v167
	ds_read_b128 v[206:209], v167 offset:16
	ds_read_b128 v[210:213], v167 offset:2048
	ds_read_b128 v[214:217], v167 offset:2064
	ds_read_b128 v[218:221], v167 offset:4096
	ds_read_b128 v[222:225], v167 offset:4112
	ds_read_b128 v[226:229], v167 offset:6144
	ds_read_b128 v[230:233], v167 offset:6160
	global_load_lds_dwordx4 v[144:145], off
	v_lshl_add_u64 v[144:145], s[42:43], 0, v[140:141]
	s_mov_b32 m0, s31
	s_nop 0
	global_load_lds_dwordx4 v[144:145], off
	s_waitcnt vmcnt(8)
	s_waitcnt lgkmcnt(0)
	s_barrier
	s_setprio 1
	s_waitcnt lgkmcnt(0)
	v_mfma_f32_16x16x128_f8f6f4 v[130:133], v[170:177], v[202:209], v[130:133]
	v_mfma_f32_16x16x128_f8f6f4 v[122:125], v[178:185], v[202:209], v[122:125]
	v_mfma_f32_16x16x128_f8f6f4 v[114:117], v[170:177], v[210:217], v[114:117]
	v_mfma_f32_16x16x128_f8f6f4 v[106:109], v[178:185], v[210:217], v[106:109]
	v_mfma_f32_16x16x128_f8f6f4 v[98:101], v[170:177], v[218:225], v[98:101]
	v_mfma_f32_16x16x128_f8f6f4 v[90:93], v[178:185], v[218:225], v[90:93]
	v_mfma_f32_16x16x128_f8f6f4 v[74:77], v[170:177], v[226:233], v[74:77]
	v_mfma_f32_16x16x128_f8f6f4 v[58:61], v[178:185], v[226:233], v[58:61]
	s_setprio 0
	s_setprio 1
	v_mfma_f32_16x16x128_f8f6f4 v[126:129], v[186:193], v[202:209], v[126:129]
	v_mfma_f32_16x16x128_f8f6f4 v[118:121], v[194:201], v[202:209], v[118:121]
	v_mfma_f32_16x16x128_f8f6f4 v[110:113], v[186:193], v[210:217], v[110:113]
	v_mfma_f32_16x16x128_f8f6f4 v[102:105], v[194:201], v[210:217], v[102:105]
	v_mfma_f32_16x16x128_f8f6f4 v[94:97], v[186:193], v[218:225], v[94:97]
	v_mfma_f32_16x16x128_f8f6f4 v[86:89], v[194:201], v[218:225], v[86:89]
	v_mfma_f32_16x16x128_f8f6f4 v[62:65], v[186:193], v[226:233], v[62:65]
	v_mfma_f32_16x16x128_f8f6f4 v[54:57], v[194:201], v[226:233], v[54:57]
	s_setprio 0
	s_barrier
	s_mov_b32 m0, s51
	v_lshl_add_u64 v[144:145], s[46:47], 0, v[136:137]
	s_add_u32 s42, s46, 0x10000
	ds_read_b128 v[202:205], v167 offset:16384
	ds_read_b128 v[206:209], v167 offset:16400
	ds_read_b128 v[210:213], v167 offset:18432
	ds_read_b128 v[214:217], v167 offset:18448
	ds_read_b128 v[218:221], v167 offset:20480
	ds_read_b128 v[222:225], v167 offset:20496
	ds_read_b128 v[226:229], v167 offset:22528
	ds_read_b128 v[230:233], v167 offset:22544
	global_load_lds_dwordx4 v[144:145], off
	v_lshl_add_u64 v[146:147], s[46:47], 0, v[138:139]
	s_mov_b32 m0, s52
	s_addc_u32 s43, s47, 0
	global_load_lds_dwordx4 v[146:147], off
	v_lshl_add_u64 v[148:149], s[42:43], 0, v[136:137]
	s_mov_b32 m0, s53
	v_lshl_add_u64 v[234:235], s[48:49], 0, v[140:141]
	global_load_lds_dwordx4 v[148:149], off
	v_lshl_add_u64 v[148:149], s[42:43], 0, v[138:139]
	s_mov_b32 m0, s55
	s_nop 0
	global_load_lds_dwordx4 v[148:149], off
	v_lshl_add_u64 v[148:149], s[48:49], 0, v[134:135]
	s_mov_b32 m0, s13
	s_nop 0
	global_load_lds_dwordx4 v[148:149], off
	s_mov_b32 m0, s57
	s_nop 0
	global_load_lds_dwordx4 v[234:235], off
	s_waitcnt vmcnt(8)
	s_waitcnt lgkmcnt(0)
	s_barrier
	s_setprio 1
	s_waitcnt lgkmcnt(0)
	v_mfma_f32_16x16x128_f8f6f4 v[82:85], v[170:177], v[202:209], v[82:85]
	v_mfma_f32_16x16x128_f8f6f4 v[70:73], v[178:185], v[202:209], v[70:73]
	v_mfma_f32_16x16x128_f8f6f4 v[50:53], v[170:177], v[210:217], v[50:53]
	v_mfma_f32_16x16x128_f8f6f4 v[42:45], v[178:185], v[210:217], v[42:45]
	v_mfma_f32_16x16x128_f8f6f4 v[34:37], v[170:177], v[218:225], v[34:37]
	v_mfma_f32_16x16x128_f8f6f4 v[26:29], v[178:185], v[218:225], v[26:29]
	v_mfma_f32_16x16x128_f8f6f4 v[18:21], v[170:177], v[226:233], v[18:21]
	v_mfma_f32_16x16x128_f8f6f4 v[10:13], v[178:185], v[226:233], v[10:13]
	s_setprio 0
	s_setprio 1
	v_mfma_f32_16x16x128_f8f6f4 v[78:81], v[186:193], v[202:209], v[78:81]
	v_mfma_f32_16x16x128_f8f6f4 v[66:69], v[194:201], v[202:209], v[66:69]
	v_mfma_f32_16x16x128_f8f6f4 v[46:49], v[186:193], v[210:217], v[46:49]
	v_mfma_f32_16x16x128_f8f6f4 v[38:41], v[194:201], v[210:217], v[38:41]
	v_mfma_f32_16x16x128_f8f6f4 v[30:33], v[186:193], v[218:225], v[30:33]
	v_mfma_f32_16x16x128_f8f6f4 v[22:25], v[194:201], v[218:225], v[22:25]
	v_mfma_f32_16x16x128_f8f6f4 v[14:17], v[186:193], v[226:233], v[14:17]
	v_mfma_f32_16x16x128_f8f6f4 v[6:9], v[194:201], v[226:233], v[6:9]
	s_setprio 0
	s_barrier
	ds_read_b128 v[174:177], v161
	ds_read_b128 v[178:181], v162
	ds_read_b128 v[170:173], v153
	ds_read_b128 v[186:189], v154
	ds_read_b128 v[182:185], v163
	ds_read_b128 v[190:193], v164
	ds_read_b128 v[194:197], v165
	ds_read_b128 v[198:201], v166
	s_add_u32 s42, s48, 0x10000
	s_addc_u32 s43, s49, 0
	s_mov_b32 m0, s58
	v_lshl_add_u64 v[236:237], s[42:43], 0, v[134:135]
	ds_read_b128 v[202:205], v167 offset:32768
	ds_read_b128 v[206:209], v167 offset:32784
	ds_read_b128 v[210:213], v167 offset:34816
	ds_read_b128 v[214:217], v167 offset:34832
	ds_read_b128 v[218:221], v167 offset:36864
	ds_read_b128 v[222:225], v167 offset:36880
	ds_read_b128 v[226:229], v167 offset:38912
	ds_read_b128 v[230:233], v167 offset:38928
	global_load_lds_dwordx4 v[236:237], off
	v_lshl_add_u64 v[236:237], s[42:43], 0, v[140:141]
	s_mov_b32 m0, s59
	s_nop 0
	global_load_lds_dwordx4 v[236:237], off
	s_waitcnt vmcnt(8)
	s_waitcnt lgkmcnt(0)
	s_barrier
	s_setprio 1
	s_waitcnt lgkmcnt(0)
	v_mfma_f32_16x16x128_f8f6f4 v[130:133], v[170:177], v[202:209], v[130:133]
	v_mfma_f32_16x16x128_f8f6f4 v[122:125], v[178:185], v[202:209], v[122:125]
	v_mfma_f32_16x16x128_f8f6f4 v[114:117], v[170:177], v[210:217], v[114:117]
	v_mfma_f32_16x16x128_f8f6f4 v[106:109], v[178:185], v[210:217], v[106:109]
	v_mfma_f32_16x16x128_f8f6f4 v[98:101], v[170:177], v[218:225], v[98:101]
	v_mfma_f32_16x16x128_f8f6f4 v[90:93], v[178:185], v[218:225], v[90:93]
	v_mfma_f32_16x16x128_f8f6f4 v[74:77], v[170:177], v[226:233], v[74:77]
	v_mfma_f32_16x16x128_f8f6f4 v[58:61], v[178:185], v[226:233], v[58:61]
	s_setprio 0
	s_setprio 1
	v_mfma_f32_16x16x128_f8f6f4 v[126:129], v[186:193], v[202:209], v[126:129]
	v_mfma_f32_16x16x128_f8f6f4 v[118:121], v[194:201], v[202:209], v[118:121]
	v_mfma_f32_16x16x128_f8f6f4 v[110:113], v[186:193], v[210:217], v[110:113]
	v_mfma_f32_16x16x128_f8f6f4 v[102:105], v[194:201], v[210:217], v[102:105]
	v_mfma_f32_16x16x128_f8f6f4 v[94:97], v[186:193], v[218:225], v[94:97]
	v_mfma_f32_16x16x128_f8f6f4 v[86:89], v[194:201], v[218:225], v[86:89]
	v_mfma_f32_16x16x128_f8f6f4 v[62:65], v[186:193], v[226:233], v[62:65]
	v_mfma_f32_16x16x128_f8f6f4 v[54:57], v[194:201], v[226:233], v[54:57]
	s_setprio 0
	s_barrier
	s_mov_b32 m0, s61
	v_lshl_add_u64 v[144:145], v[144:145], 0, s[20:21]
	s_add_u32 s42, s46, 0x10080
	ds_read_b128 v[202:205], v167 offset:49152
	ds_read_b128 v[206:209], v167 offset:49168
	ds_read_b128 v[210:213], v167 offset:51200
	ds_read_b128 v[214:217], v167 offset:51216
	ds_read_b128 v[218:221], v167 offset:53248
	ds_read_b128 v[222:225], v167 offset:53264
	ds_read_b128 v[226:229], v167 offset:55296
	ds_read_b128 v[230:233], v167 offset:55312
	global_load_lds_dwordx4 v[144:145], off
	v_lshl_add_u64 v[144:145], v[146:147], 0, s[20:21]
	s_mov_b32 m0, s62
	s_addc_u32 s43, s47, 0
	global_load_lds_dwordx4 v[144:145], off
	v_lshl_add_u64 v[144:145], s[42:43], 0, v[136:137]
	s_mov_b32 m0, s65
	s_nop 0
	global_load_lds_dwordx4 v[144:145], off
	v_lshl_add_u64 v[144:145], s[42:43], 0, v[138:139]
	s_mov_b32 m0, s66
	s_nop 0
	global_load_lds_dwordx4 v[144:145], off
	v_lshl_add_u64 v[144:145], v[148:149], 0, s[20:21]
	s_mov_b32 m0, s63
	s_nop 0
	global_load_lds_dwordx4 v[144:145], off
	v_lshl_add_u64 v[144:145], v[234:235], 0, s[20:21]
	s_mov_b32 m0, s64
	s_nop 0
	global_load_lds_dwordx4 v[144:145], off
	s_waitcnt vmcnt(8)
	s_waitcnt lgkmcnt(0)
	s_barrier
	s_setprio 1
	s_waitcnt lgkmcnt(0)
	v_mfma_f32_16x16x128_f8f6f4 v[82:85], v[170:177], v[202:209], v[82:85]
	v_mfma_f32_16x16x128_f8f6f4 v[70:73], v[178:185], v[202:209], v[70:73]
	v_mfma_f32_16x16x128_f8f6f4 v[50:53], v[170:177], v[210:217], v[50:53]
	v_mfma_f32_16x16x128_f8f6f4 v[42:45], v[178:185], v[210:217], v[42:45]
	v_mfma_f32_16x16x128_f8f6f4 v[34:37], v[170:177], v[218:225], v[34:37]
	v_mfma_f32_16x16x128_f8f6f4 v[26:29], v[178:185], v[218:225], v[26:29]
	v_mfma_f32_16x16x128_f8f6f4 v[18:21], v[170:177], v[226:233], v[18:21]
	v_mfma_f32_16x16x128_f8f6f4 v[10:13], v[178:185], v[226:233], v[10:13]
	s_setprio 0
	s_setprio 1
	v_mfma_f32_16x16x128_f8f6f4 v[78:81], v[186:193], v[202:209], v[78:81]
	v_mfma_f32_16x16x128_f8f6f4 v[66:69], v[194:201], v[202:209], v[66:69]
	v_mfma_f32_16x16x128_f8f6f4 v[46:49], v[186:193], v[210:217], v[46:49]
	v_mfma_f32_16x16x128_f8f6f4 v[38:41], v[194:201], v[210:217], v[38:41]
	v_mfma_f32_16x16x128_f8f6f4 v[30:33], v[186:193], v[218:225], v[30:33]
	v_mfma_f32_16x16x128_f8f6f4 v[22:25], v[194:201], v[218:225], v[22:25]
	v_mfma_f32_16x16x128_f8f6f4 v[14:17], v[186:193], v[226:233], v[14:17]
	v_mfma_f32_16x16x128_f8f6f4 v[6:9], v[194:201], v[226:233], v[6:9]
	s_setprio 0
	s_barrier
	s_andn2_b64 vcc, exec, s[22:23]
	s_cbranch_vccnz .LBB0_4279
	s_barrier
